# add GEMM2 epilogue per-path waits and hoisted layer-0 gain loads on top of v21
# speedup vs baseline: 1.0112x; 1.0112x over previous
.LBB0_567:
	s_and_b64 vcc, exec, s[10:11]
	s_cbranch_vccz .LBB0_590
	s_ashr_i32 s9, s8, 31
	v_readlane_b32 s12, v251, 18
	s_lshl_b64 s[0:1], s[8:9], 13
	v_readlane_b32 s14, v251, 20
	v_lshlrev_b32_e32 v6, 4, v68
	v_readlane_b32 s15, v251, 21
	s_add_u32 s2, s14, s0
	v_ashrrev_i32_e32 v7, 31, v6
	v_readlane_b32 s24, v251, 30
	s_addc_u32 s3, s15, s1
	v_lshlrev_b64 v[8:9], 2, v[6:7]
	v_readlane_b32 s16, v251, 22
	v_lshl_add_u64 v[0:1], s[2:3], 0, v[8:9]
	s_mov_b64 s[10:11], 0x1000
	s_movk_i32 s24, 0x1000
	v_readlane_b32 s17, v251, 23
	global_load_dwordx4 v[108:111], v[0:1], off offset:48
	global_load_dwordx4 v[116:119], v[0:1], off offset:32
	global_load_dwordx4 v[120:123], v[0:1], off offset:16
	global_load_dwordx4 v[124:127], v[0:1], off
	v_lshl_add_u64 v[2:3], v[0:1], 0, s[10:11]
	v_add_co_u32_e32 v0, vcc, s24, v0
	s_add_u32 s0, s16, s0
	s_nop 0
	v_addc_co_u32_e32 v1, vcc, 0, v1, vcc
	s_addc_u32 s1, s17, s1
	global_load_dwordx4 v[112:115], v[0:1], off
	global_load_dwordx4 v[96:99], v[2:3], off offset:48
	global_load_dwordx4 v[100:103], v[2:3], off offset:32
	global_load_dwordx4 v[104:107], v[2:3], off offset:16
	v_lshl_add_u64 v[0:1], s[0:1], 0, v[8:9]
	global_load_dwordx4 v[64:67], v[0:1], off offset:48
	global_load_dwordx4 v[84:87], v[0:1], off offset:32
	global_load_dwordx4 v[88:91], v[0:1], off offset:16
	global_load_dwordx4 v[92:95], v[0:1], off
	v_lshl_add_u64 v[10:11], v[0:1], 0, s[10:11]
	v_add_co_u32_e32 v0, vcc, s24, v0
	v_lshl_add_u64 v[132:133], s[84:85], 0, v[8:9]
	s_nop 0
	v_addc_co_u32_e32 v1, vcc, 0, v1, vcc
	global_load_dwordx4 v[80:83], v[0:1], off
	s_nop 0
	global_load_dwordx4 v[0:3], v[10:11], off offset:48
	global_load_dwordx4 v[16:19], v[10:11], off offset:32
	global_load_dwordx4 v[40:43], v[10:11], off offset:16
	v_and_b32_e32 v10, 0x70, v6
	v_add_u32_e32 v6, 0x400, v6
	s_mov_b64 s[2:3], 0x1010
	v_ashrrev_i32_e32 v6, 7, v6
	v_lshl_add_u64 v[136:137], v[132:133], 0, s[2:3]
	s_mov_b64 s[2:3], 0x1020
	v_readlane_b32 s13, v251, 19
	v_ashrrev_i32_e32 v5, 31, v4
	v_ashrrev_i32_e32 v7, 31, v6
	s_cmp_lg_u64 s[84:85], 0
	v_lshl_add_u64 v[138:139], v[132:133], 0, s[2:3]
	s_mov_b64 s[2:3], 0x1030
	v_lshlrev_b64 v[4:5], 21, v[4:5]
	v_lshlrev_b64 v[6:7], 21, v[6:7]
	s_cselect_b64 s[12:13], -1, 0
	v_lshl_add_u64 v[140:141], v[132:133], 0, s[2:3]
	s_lshl_b64 s[2:3], s[8:9], 7
	v_readlane_b32 s18, v251, 24
	v_readlane_b32 s19, v251, 25
	v_readlane_b32 s25, v251, 31
	v_readlane_b32 s26, v251, 32
	s_ashr_i32 s7, s6, 31
	v_lshl_add_u64 v[142:143], v[4:5], 0, s[2:3]
	v_lshl_add_u64 v[144:145], v[6:7], 0, s[2:3]
	v_cmp_eq_u32_e64 s[0:1], 0, v68
	v_lshl_add_u64 v[128:129], s[14:15], 0, v[8:9]
	v_lshl_add_u64 v[130:131], s[16:17], 0, v[8:9]
	v_lshl_add_u64 v[134:135], v[132:133], 0, s[10:11]
	s_lshl_b64 s[14:15], s[8:9], 2
	s_lshl_b64 s[16:17], s[6:7], 2
	v_or_b32_e32 v142, v142, v10
	s_lshl_b64 s[18:19], s[6:7], 7
	v_or_b32_e32 v144, v144, v10
	s_mov_b32 s7, 0x42fe0000
	s_mov_b32 s9, 0x40c0c00
	s_mov_b32 s25, 0x35200000
	v_mov_b32_e32 v146, 0x840000
	s_mov_b32 s26, 0x3d200000
	v_mov_b32_e32 v147, 0x880000
	v_readlane_b32 s20, v251, 26
	v_readlane_b32 s21, v251, 27
	v_readlane_b32 s22, v251, 28
	v_readlane_b32 s23, v251, 29
	v_readlane_b32 s27, v251, 33
	s_andn2_b64 vcc, exec, s[12:13]
	s_cbranch_vccnz .Lp0_nogain
	global_load_dwordx4 v[154:157], v[132:133], off
	global_load_dwordx4 v[158:161], v[132:133], off offset:16
	global_load_dwordx4 v[162:165], v[132:133], off offset:32
	global_load_dwordx4 v[166:169], v[132:133], off offset:48
	global_load_dwordx4 v[170:173], v[134:135], off
	global_load_dwordx4 v[174:177], v[136:137], off
	global_load_dwordx4 v[178:181], v[138:139], off
	global_load_dwordx4 v[182:185], v[140:141], off
.Lp0_nogain:
	s_branch .LBB0_570
.LBB0_569:
	s_or_b64 exec, exec, s[22:23]
	s_add_u32 s14, s14, s16
	s_waitcnt vmcnt(8)
	v_mov_b64_e32 v[94:95], v[58:59]
	v_mov_b64_e32 v[90:91], v[54:55]
	v_mov_b64_e32 v[86:87], v[50:51]
	v_mov_b64_e32 v[66:67], v[46:47]
	s_waitcnt vmcnt(7)
	v_mov_b64_e32 v[82:83], v[74:75]
	s_waitcnt vmcnt(4)
	v_mov_b64_e32 v[40:41], v[76:77]
	v_mov_b64_e32 v[16:17], v[68:69]
	v_mov_b64_e32 v[0:1], v[60:61]
	v_mov_b64_e32 v[126:127], v[22:23]
	v_mov_b64_e32 v[122:123], v[14:15]
	v_mov_b64_e32 v[118:119], v[10:11]
	v_mov_b64_e32 v[110:111], v[6:7]
	v_mov_b64_e32 v[114:115], v[34:35]
	v_mov_b64_e32 v[106:107], v[38:39]
	v_mov_b64_e32 v[102:103], v[30:31]
	v_mov_b64_e32 v[98:99], v[26:27]
	s_addc_u32 s15, s15, s17
	v_lshl_add_u64 v[142:143], v[142:143], 0, s[18:19]
	v_lshl_add_u64 v[144:145], v[144:145], 0, s[18:19]
	s_andn2_b64 vcc, exec, s[20:21]
	v_mov_b64_e32 v[92:93], v[56:57]
	v_mov_b64_e32 v[88:89], v[52:53]
	v_mov_b64_e32 v[84:85], v[48:49]
	v_mov_b64_e32 v[64:65], v[44:45]
	v_mov_b64_e32 v[80:81], v[72:73]
	v_mov_b64_e32 v[42:43], v[78:79]
	v_mov_b64_e32 v[18:19], v[70:71]
	v_mov_b64_e32 v[2:3], v[62:63]
	v_mov_b64_e32 v[124:125], v[20:21]
	v_mov_b64_e32 v[120:121], v[12:13]
	v_mov_b64_e32 v[116:117], v[8:9]
	v_mov_b64_e32 v[108:109], v[4:5]
	v_mov_b64_e32 v[112:113], v[32:33]
	v_mov_b64_e32 v[104:105], v[36:37]
	v_mov_b64_e32 v[100:101], v[28:29]
	v_mov_b64_e32 v[96:97], v[24:25]
	s_cbranch_vccz .LBB0_590
.LBB0_570:
	s_mov_b32 s2, s8
	s_add_i32 s8, s8, s6
	s_cmpk_gt_i32 s8, 0x3fff
	s_cselect_b64 s[20:21], -1, 0
	s_cmpk_lt_i32 s8, 0x4000
	s_cselect_b32 s2, s8, s2
	s_ashr_i32 s3, s2, 31
	s_lshl_b64 s[2:3], s[2:3], 13
	v_lshl_add_u64 v[24:25], v[128:129], 0, s[2:3]
	global_load_dwordx4 v[4:7], v[24:25], off offset:48
	global_load_dwordx4 v[8:11], v[24:25], off offset:32
	global_load_dwordx4 v[12:15], v[24:25], off offset:16
	global_load_dwordx4 v[20:23], v[24:25], off
	v_lshl_add_u64 v[36:37], v[24:25], 0, s[10:11]
	v_add_co_u32_e32 v24, vcc, s24, v24
	v_lshl_add_u64 v[60:61], v[130:131], 0, s[2:3]
	s_nop 0
	v_addc_co_u32_e32 v25, vcc, 0, v25, vcc
	global_load_dwordx4 v[32:35], v[24:25], off
	s_nop 0
	global_load_dwordx4 v[24:27], v[36:37], off offset:48
	global_load_dwordx4 v[28:31], v[36:37], off offset:32
	s_nop 0
	global_load_dwordx4 v[36:39], v[36:37], off offset:16
	s_nop 0
	global_load_dwordx4 v[44:47], v[60:61], off offset:48
	global_load_dwordx4 v[48:51], v[60:61], off offset:32
	global_load_dwordx4 v[52:55], v[60:61], off offset:16
	global_load_dwordx4 v[56:59], v[60:61], off
	v_lshl_add_u64 v[76:77], v[60:61], 0, s[10:11]
	v_add_co_u32_e32 v60, vcc, 0x1000, v60
	v_cndmask_b32_e64 v148, 0, 1, s[12:13]
	s_nop 0
	v_addc_co_u32_e32 v61, vcc, 0, v61, vcc
	global_load_dwordx4 v[72:75], v[60:61], off
	s_nop 0
	global_load_dwordx4 v[60:63], v[76:77], off offset:48
	global_load_dwordx4 v[68:71], v[76:77], off offset:32
	s_nop 0
	global_load_dwordx4 v[76:79], v[76:77], off offset:16
	s_andn2_b64 vcc, exec, s[12:13]
	s_cbranch_vccnz .LBB0_586
	s_waitcnt vmcnt(16)
	v_pk_mul_f32 v[126:127], v[126:127], v[156:157]
	v_pk_mul_f32 v[124:125], v[124:125], v[154:155]
	v_pk_mul_f32 v[122:123], v[122:123], v[160:161]
	v_pk_mul_f32 v[120:121], v[120:121], v[158:159]
	v_pk_mul_f32 v[118:119], v[118:119], v[164:165]
	v_pk_mul_f32 v[116:117], v[116:117], v[162:163]
	v_pk_mul_f32 v[110:111], v[110:111], v[168:169]
	v_pk_mul_f32 v[108:109], v[108:109], v[166:167]
	v_pk_mul_f32 v[114:115], v[114:115], v[172:173]
	v_pk_mul_f32 v[112:113], v[112:113], v[170:171]
	v_pk_mul_f32 v[106:107], v[106:107], v[176:177]
	v_pk_mul_f32 v[104:105], v[104:105], v[174:175]
	v_pk_mul_f32 v[102:103], v[102:103], v[180:181]
	v_pk_mul_f32 v[100:101], v[100:101], v[178:179]
	v_pk_mul_f32 v[98:99], v[98:99], v[184:185]
	v_pk_mul_f32 v[96:97], v[96:97], v[182:183]

.LBB0_1601:
	v_cndmask_b32_e64 v192, 0, 1, s[14:15]
	s_mov_b64 s[24:25], -1
	v_cmp_ne_u32_e64 s[6:7], 1, v192
	s_andn2_b64 vcc, exec, s[14:15]
	v_lshl_add_u64 v[222:223], v[218:219], 2, s[8:9]
	s_cbranch_vccnz .LBB0_1603
	global_load_dwordx4 v[196:199], v[222:223], off offset:16
	global_load_dwordx4 v[192:195], v[222:223], off
	s_waitcnt vmcnt(0)
	s_mov_b64 s[24:25], 0
.LBB0_1603:
	s_andn2_b64 vcc, exec, s[24:25]
	s_cbranch_vccnz .LBB0_1605
	s_waitcnt vmcnt(15)
	v_lshlrev_b32_e32 v192, 16, v188
	v_and_b32_e32 v193, 0xffff0000, v188
	v_lshlrev_b32_e32 v194, 16, v189
	v_and_b32_e32 v195, 0xffff0000, v189
	v_lshlrev_b32_e32 v196, 16, v190
	v_and_b32_e32 v197, 0xffff0000, v190
	v_lshlrev_b32_e32 v198, 16, v191
	v_and_b32_e32 v199, 0xffff0000, v191
.LBB0_1605:
	v_pk_add_f32 v[190:191], v[158:159], v[194:195]
	v_pk_add_f32 v[194:195], v[156:157], v[192:193]
	v_pk_add_f32 v[188:189], v[154:155], v[198:199]
	v_pk_add_f32 v[192:193], v[152:153], v[196:197]
	v_cvt_pk_bf16_f32 v152, v194, v195
	v_cvt_pk_bf16_f32 v153, v190, v191
	s_and_b64 vcc, exec, s[6:7]
	v_cvt_pk_bf16_f32 v154, v192, v193
	v_cvt_pk_bf16_f32 v155, v188, v189
	s_mov_b64 s[24:25], -1
	global_store_dwordx4 v[220:221], v[152:155], off
	s_cbranch_vccnz .LBB0_1607
	global_load_dwordx4 v[156:159], v[222:223], off offset:528
	global_load_dwordx4 v[152:155], v[222:223], off offset:512
	s_waitcnt vmcnt(0)
	s_mov_b64 s[24:25], 0
.LBB0_1607:
	s_andn2_b64 vcc, exec, s[24:25]
	s_cbranch_vccnz .LBB0_1609
	s_waitcnt vmcnt(15)
	v_lshlrev_b32_e32 v152, 16, v184
	v_and_b32_e32 v153, 0xffff0000, v184
	v_lshlrev_b32_e32 v154, 16, v185
	v_and_b32_e32 v155, 0xffff0000, v185
	v_lshlrev_b32_e32 v156, 16, v186
	v_and_b32_e32 v157, 0xffff0000, v186
	v_lshlrev_b32_e32 v158, 16, v187
	v_and_b32_e32 v159, 0xffff0000, v187
.LBB0_1609:
	v_pk_add_f32 v[146:147], v[146:147], v[154:155]
	v_pk_add_f32 v[144:145], v[144:145], v[152:153]
	v_pk_add_f32 v[154:155], v[136:137], v[156:157]
	v_cvt_pk_bf16_f32 v136, v144, v145
	v_cvt_pk_bf16_f32 v137, v146, v147
	v_mul_f32_e32 v184, v195, v195
	v_mul_f32_e32 v185, v191, v191
	v_pk_add_f32 v[152:153], v[138:139], v[158:159]
	v_cvt_pk_bf16_f32 v138, v154, v155
	v_fmac_f32_e32 v184, v194, v194
	v_cvt_pk_bf16_f32 v139, v152, v153
	global_store_dwordx4 v[220:221], v[136:139], off offset:256
	v_fmac_f32_e32 v185, v190, v190
	v_add_f32_e32 v184, v184, v185
	v_mul_f32_e32 v136, v145, v145
	v_mul_f32_e32 v137, v147, v147
	v_fmac_f32_e32 v136, v144, v144
	v_fmac_f32_e32 v137, v146, v146
	v_mul_f32_e32 v185, v193, v193
	v_add_f32_e32 v136, v136, v137
	v_mul_f32_e32 v137, v155, v155
	v_fmac_f32_e32 v185, v192, v192
	v_fmac_f32_e32 v137, v154, v154
	v_add_f32_e32 v184, v185, v184
	v_mul_f32_e32 v185, v189, v189
	v_add_f32_e32 v136, v137, v136
	v_mul_f32_e32 v137, v153, v153
	v_fmac_f32_e32 v185, v188, v188
	v_fmac_f32_e32 v137, v152, v152
	v_add_f32_e32 v184, v185, v184
	v_add_f32_e32 v136, v137, v136
	v_add_f32_e32 v136, v184, v136
	v_mov_b32_e32 v137, v136
	s_nop 1
	v_permlane16_swap_b32_e32 v136, v137
	v_add_f32_e32 v136, v136, v137
	s_lshl_b32 s24, s42, 2
	v_mov_b32_e32 v137, v136
	s_ashr_i32 s25, s24, 31
	s_nop 0
	v_permlane32_swap_b32_e32 v136, v137
	s_and_saveexec_b64 s[26:27], s[4:5]
	s_cbranch_execz .LBB0_1611
	v_lshlrev_b64 v[138:139], 7, v[216:217]
	v_lshl_add_u64 v[138:139], s[66:67], 0, v[138:139]
	v_lshl_add_u64 v[138:139], s[24:25], 2, v[138:139]
	s_lshl_b32 s94, s38, 2
	v_lshl_add_u64 v[138:139], v[138:139], 0, s[94:95]
	v_add_f32_e32 v136, v136, v137
	global_store_dword v[138:139], v136, off
.LBB0_1611:
	s_or_b64 exec, exec, s[26:27]
	s_mov_b64 s[0:1], 0x8000
	v_lshl_add_u64 v[156:157], v[218:219], 0, s[0:1]
	s_mov_b64 s[26:27], -1
	s_and_b64 vcc, exec, s[6:7]
	v_lshl_add_u64 v[152:153], v[156:157], 2, s[8:9]
	s_cbranch_vccnz .LBB0_1613
	global_load_dwordx4 v[144:147], v[152:153], off offset:16
	global_load_dwordx4 v[136:139], v[152:153], off
	s_waitcnt vmcnt(0)
	s_mov_b64 s[26:27], 0
.LBB0_1613:
	s_andn2_b64 vcc, exec, s[26:27]
	s_cbranch_vccnz .LBB0_1615
	s_waitcnt vmcnt(16)
	v_lshlrev_b32_e32 v136, 16, v180
	v_and_b32_e32 v137, 0xffff0000, v180
	v_lshlrev_b32_e32 v138, 16, v181
	v_and_b32_e32 v139, 0xffff0000, v181
	v_lshlrev_b32_e32 v144, 16, v182
	v_and_b32_e32 v145, 0xffff0000, v182
	v_lshlrev_b32_e32 v146, 16, v183
	v_and_b32_e32 v147, 0xffff0000, v183
.LBB0_1615:
	v_pk_add_f32 v[154:155], v[134:135], v[138:139]
	v_pk_add_f32 v[158:159], v[132:133], v[136:137]
	v_pk_add_f32 v[138:139], v[126:127], v[146:147]
	v_pk_add_f32 v[144:145], v[124:125], v[144:145]
	v_cvt_pk_bf16_f32 v124, v158, v159
	v_cvt_pk_bf16_f32 v125, v154, v155
	v_lshl_add_u64 v[136:137], v[156:157], 1, s[70:71]
	v_cvt_pk_bf16_f32 v126, v144, v145
	v_cvt_pk_bf16_f32 v127, v138, v139
	s_and_b64 vcc, exec, s[6:7]
	s_mov_b64 s[26:27], -1
	global_store_dwordx4 v[136:137], v[124:127], off
	s_cbranch_vccnz .LBB0_1617
	global_load_dwordx4 v[132:135], v[152:153], off offset:528
	global_load_dwordx4 v[124:127], v[152:153], off offset:512
	s_waitcnt vmcnt(0)
	s_mov_b64 s[26:27], 0
.LBB0_1617:
	s_andn2_b64 vcc, exec, s[26:27]
	s_cbranch_vccnz .LBB0_1619
	s_waitcnt vmcnt(16)
	v_lshlrev_b32_e32 v124, 16, v176
	v_and_b32_e32 v125, 0xffff0000, v176
	v_lshlrev_b32_e32 v126, 16, v177
	v_and_b32_e32 v127, 0xffff0000, v177
	v_lshlrev_b32_e32 v132, 16, v178
	v_and_b32_e32 v133, 0xffff0000, v178
	v_lshlrev_b32_e32 v134, 16, v179
	v_and_b32_e32 v135, 0xffff0000, v179
.LBB0_1619:
	v_pk_add_f32 v[118:119], v[118:119], v[126:127]
	v_pk_add_f32 v[116:117], v[116:117], v[124:125]
	v_pk_add_f32 v[126:127], v[112:113], v[132:133]
	v_cvt_pk_bf16_f32 v112, v116, v117
	v_cvt_pk_bf16_f32 v113, v118, v119
	v_pk_add_f32 v[124:125], v[114:115], v[134:135]
	v_cvt_pk_bf16_f32 v114, v126, v127
	v_mul_f32_e32 v146, v159, v159
	v_cvt_pk_bf16_f32 v115, v124, v125
	global_store_dwordx4 v[136:137], v[112:115], off offset:256
	v_mul_f32_e32 v147, v155, v155
	v_fmac_f32_e32 v146, v158, v158
	v_mul_f32_e32 v112, v117, v117
	v_mul_f32_e32 v113, v119, v119
	v_fmac_f32_e32 v112, v116, v116
	v_fmac_f32_e32 v113, v118, v118
	v_add_f32_e32 v112, v112, v113
	v_mul_f32_e32 v113, v127, v127
	v_fmac_f32_e32 v147, v154, v154
	v_mul_f32_e32 v145, v145, v145
	v_fmac_f32_e32 v113, v126, v126
	v_add_f32_e32 v146, v146, v147
	v_fmac_f32_e32 v145, v144, v144
	v_mul_f32_e32 v139, v139, v139
	v_add_f32_e32 v112, v113, v112
	v_mul_f32_e32 v113, v125, v125
	v_add_f32_e32 v144, v145, v146
	v_fmac_f32_e32 v139, v138, v138
	v_fmac_f32_e32 v113, v124, v124
	v_add_f32_e32 v138, v139, v144
	v_add_f32_e32 v112, v113, v112
	v_add_f32_e32 v112, v138, v112
	v_mov_b32_e32 v113, v112
	s_nop 1
	v_permlane16_swap_b32_e32 v112, v113
	v_add_f32_e32 v112, v112, v113
	v_mov_b32_e32 v113, v112
	s_nop 1
	v_permlane32_swap_b32_e32 v112, v113
	s_and_saveexec_b64 s[26:27], s[4:5]
	s_cbranch_execz .LBB0_1621
	v_or_b32_e32 v114, 16, v216
	v_ashrrev_i32_e32 v115, 31, v114
	v_add_f32_e32 v116, v112, v113
	v_lshlrev_b64 v[112:113], 7, v[114:115]
	v_lshl_add_u64 v[112:113], s[66:67], 0, v[112:113]
	v_lshl_add_u64 v[112:113], s[24:25], 2, v[112:113]
	s_lshl_b32 s94, s38, 2
	v_lshl_add_u64 v[112:113], v[112:113], 0, s[94:95]
	global_store_dword v[112:113], v116, off
.LBB0_1621:
	s_or_b64 exec, exec, s[26:27]
	s_mov_b64 s[0:1], 0x10000
	v_lshl_add_u64 v[132:133], v[218:219], 0, s[0:1]
	s_mov_b64 s[26:27], -1
	s_and_b64 vcc, exec, s[6:7]
	v_lshl_add_u64 v[124:125], v[132:133], 2, s[8:9]
	s_cbranch_vccnz .LBB0_1623
	global_load_dwordx4 v[116:119], v[124:125], off offset:16
	global_load_dwordx4 v[112:115], v[124:125], off
	s_waitcnt vmcnt(0)
	s_mov_b64 s[26:27], 0
.LBB0_1623:
	s_andn2_b64 vcc, exec, s[26:27]
	s_cbranch_vccnz .LBB0_1625
	s_waitcnt vmcnt(17)
	v_lshlrev_b32_e32 v112, 16, v172
	v_and_b32_e32 v113, 0xffff0000, v172
	v_lshlrev_b32_e32 v114, 16, v173
	v_and_b32_e32 v115, 0xffff0000, v173
	v_lshlrev_b32_e32 v116, 16, v174
	v_and_b32_e32 v117, 0xffff0000, v174
	v_lshlrev_b32_e32 v118, 16, v175
	v_and_b32_e32 v119, 0xffff0000, v175
.LBB0_1625:
	v_pk_add_f32 v[126:127], v[106:107], v[114:115]
	v_pk_add_f32 v[134:135], v[104:105], v[112:113]
	v_pk_add_f32 v[114:115], v[102:103], v[118:119]
	v_pk_add_f32 v[116:117], v[100:101], v[116:117]
	v_cvt_pk_bf16_f32 v100, v134, v135
	v_cvt_pk_bf16_f32 v101, v126, v127
	v_lshl_add_u64 v[112:113], v[132:133], 1, s[70:71]
	v_cvt_pk_bf16_f32 v102, v116, v117
	v_cvt_pk_bf16_f32 v103, v114, v115
	s_and_b64 vcc, exec, s[6:7]
	s_mov_b64 s[26:27], -1
	global_store_dwordx4 v[112:113], v[100:103], off
	s_cbranch_vccnz .LBB0_1627
	global_load_dwordx4 v[104:107], v[124:125], off offset:528
	global_load_dwordx4 v[100:103], v[124:125], off offset:512
	s_waitcnt vmcnt(0)
	s_mov_b64 s[26:27], 0
.LBB0_1627:
	s_andn2_b64 vcc, exec, s[26:27]
	s_cbranch_vccnz .LBB0_1629
	s_waitcnt vmcnt(17)
	v_lshlrev_b32_e32 v100, 16, v168
	v_and_b32_e32 v101, 0xffff0000, v168
	v_lshlrev_b32_e32 v102, 16, v169
	v_and_b32_e32 v103, 0xffff0000, v169
	v_lshlrev_b32_e32 v104, 16, v170
	v_and_b32_e32 v105, 0xffff0000, v170
	v_lshlrev_b32_e32 v106, 16, v171
	v_and_b32_e32 v107, 0xffff0000, v171
.LBB0_1629:
	v_pk_add_f32 v[94:95], v[94:95], v[102:103]
	v_pk_add_f32 v[92:93], v[92:93], v[100:101]
	v_pk_add_f32 v[102:103], v[84:85], v[104:105]
	v_cvt_pk_bf16_f32 v84, v92, v93
	v_cvt_pk_bf16_f32 v85, v94, v95
	v_pk_add_f32 v[100:101], v[86:87], v[106:107]
	v_cvt_pk_bf16_f32 v86, v102, v103
	v_mul_f32_e32 v118, v135, v135
	v_cvt_pk_bf16_f32 v87, v100, v101
	global_store_dwordx4 v[112:113], v[84:87], off offset:256
	v_mul_f32_e32 v119, v127, v127
	v_fmac_f32_e32 v118, v134, v134
	v_mul_f32_e32 v84, v93, v93
	v_mul_f32_e32 v85, v95, v95
	v_fmac_f32_e32 v84, v92, v92
	v_fmac_f32_e32 v85, v94, v94
	v_add_f32_e32 v84, v84, v85
	v_mul_f32_e32 v85, v103, v103
	v_fmac_f32_e32 v119, v126, v126
	v_mul_f32_e32 v117, v117, v117
	v_fmac_f32_e32 v85, v102, v102
	v_add_f32_e32 v118, v118, v119
	v_fmac_f32_e32 v117, v116, v116
	v_mul_f32_e32 v115, v115, v115
	v_add_f32_e32 v84, v85, v84
	v_mul_f32_e32 v85, v101, v101
	v_add_f32_e32 v116, v117, v118
	v_fmac_f32_e32 v115, v114, v114
	v_fmac_f32_e32 v85, v100, v100
	v_add_f32_e32 v114, v115, v116
	v_add_f32_e32 v84, v85, v84
	v_add_f32_e32 v84, v114, v84
	v_mov_b32_e32 v85, v84
	s_nop 1
	v_permlane16_swap_b32_e32 v84, v85
	v_add_f32_e32 v84, v84, v85
	v_mov_b32_e32 v85, v84
	s_nop 1
	v_permlane32_swap_b32_e32 v84, v85
	s_and_saveexec_b64 s[26:27], s[4:5]
	s_cbranch_execz .LBB0_1631
	v_or_b32_e32 v86, 32, v216
	v_ashrrev_i32_e32 v87, 31, v86
	v_add_f32_e32 v92, v84, v85
	v_lshlrev_b64 v[84:85], 7, v[86:87]
	v_lshl_add_u64 v[84:85], s[66:67], 0, v[84:85]
	v_lshl_add_u64 v[84:85], s[24:25], 2, v[84:85]
	s_lshl_b32 s94, s38, 2
	v_lshl_add_u64 v[84:85], v[84:85], 0, s[94:95]
	global_store_dword v[84:85], v92, off
.LBB0_1631:
	s_or_b64 exec, exec, s[26:27]
	s_mov_b64 s[0:1], 0x18000
	v_lshl_add_u64 v[104:105], v[218:219], 0, s[0:1]
	s_mov_b64 s[26:27], -1
	s_and_b64 vcc, exec, s[6:7]
	v_lshl_add_u64 v[100:101], v[104:105], 2, s[8:9]
	s_cbranch_vccnz .LBB0_1633
	global_load_dwordx4 v[92:95], v[100:101], off offset:16
	global_load_dwordx4 v[84:87], v[100:101], off
	s_waitcnt vmcnt(0)
	s_mov_b64 s[26:27], 0
.LBB0_1633:
	s_andn2_b64 vcc, exec, s[26:27]
	s_cbranch_vccnz .LBB0_1635
	s_waitcnt vmcnt(18)
	v_lshlrev_b32_e32 v84, 16, v164
	v_and_b32_e32 v85, 0xffff0000, v164
	v_lshlrev_b32_e32 v86, 16, v165
	v_and_b32_e32 v87, 0xffff0000, v165
	v_lshlrev_b32_e32 v92, 16, v166
	v_and_b32_e32 v93, 0xffff0000, v166
	v_lshlrev_b32_e32 v94, 16, v167
	v_and_b32_e32 v95, 0xffff0000, v167
.LBB0_1635:
	v_pk_add_f32 v[102:103], v[78:79], v[86:87]
	v_pk_add_f32 v[106:107], v[76:77], v[84:85]
	v_pk_add_f32 v[86:87], v[74:75], v[94:95]
	v_pk_add_f32 v[92:93], v[72:73], v[92:93]
	v_cvt_pk_bf16_f32 v72, v106, v107
	v_cvt_pk_bf16_f32 v73, v102, v103
	v_lshl_add_u64 v[84:85], v[104:105], 1, s[70:71]
	v_cvt_pk_bf16_f32 v74, v92, v93
	v_cvt_pk_bf16_f32 v75, v86, v87
	s_and_b64 vcc, exec, s[6:7]
	s_mov_b64 s[26:27], -1
	global_store_dwordx4 v[84:85], v[72:75], off
	s_cbranch_vccnz .LBB0_1637
	global_load_dwordx4 v[76:79], v[100:101], off offset:528
	global_load_dwordx4 v[72:75], v[100:101], off offset:512
	s_waitcnt vmcnt(0)
	s_mov_b64 s[26:27], 0
.LBB0_1637:
	s_andn2_b64 vcc, exec, s[26:27]
	s_cbranch_vccnz .LBB0_1639
	s_waitcnt vmcnt(18)
	v_lshlrev_b32_e32 v72, 16, v160
	v_and_b32_e32 v73, 0xffff0000, v160
	v_lshlrev_b32_e32 v74, 16, v161
	v_and_b32_e32 v75, 0xffff0000, v161
	v_lshlrev_b32_e32 v76, 16, v162
	v_and_b32_e32 v77, 0xffff0000, v162
	v_lshlrev_b32_e32 v78, 16, v163
	v_and_b32_e32 v79, 0xffff0000, v163
.LBB0_1639:
	v_pk_add_f32 v[70:71], v[70:71], v[74:75]
	v_pk_add_f32 v[68:69], v[68:69], v[72:73]
	v_pk_add_f32 v[74:75], v[64:65], v[76:77]
	v_cvt_pk_bf16_f32 v64, v68, v69
	v_cvt_pk_bf16_f32 v65, v70, v71
	v_pk_add_f32 v[72:73], v[66:67], v[78:79]
	v_cvt_pk_bf16_f32 v66, v74, v75
	v_mul_f32_e32 v94, v107, v107
	v_cvt_pk_bf16_f32 v67, v72, v73
	global_store_dwordx4 v[84:85], v[64:67], off offset:256
	v_mul_f32_e32 v95, v103, v103
	v_fmac_f32_e32 v94, v106, v106
	v_mul_f32_e32 v64, v69, v69
	v_mul_f32_e32 v65, v71, v71
	v_fmac_f32_e32 v64, v68, v68
	v_fmac_f32_e32 v65, v70, v70
	v_add_f32_e32 v64, v64, v65
	v_mul_f32_e32 v65, v75, v75
	v_fmac_f32_e32 v95, v102, v102
	v_mul_f32_e32 v93, v93, v93
	v_fmac_f32_e32 v65, v74, v74
	v_add_f32_e32 v94, v94, v95
	v_fmac_f32_e32 v93, v92, v92
	v_mul_f32_e32 v87, v87, v87
	v_add_f32_e32 v64, v65, v64
	v_mul_f32_e32 v65, v73, v73
	v_add_f32_e32 v92, v93, v94
	v_fmac_f32_e32 v87, v86, v86
	v_fmac_f32_e32 v65, v72, v72
	v_add_f32_e32 v86, v87, v92
	v_add_f32_e32 v64, v65, v64
	v_add_f32_e32 v64, v86, v64
	v_mov_b32_e32 v65, v64
	s_nop 1
	v_permlane16_swap_b32_e32 v64, v65
	v_add_f32_e32 v64, v64, v65
	v_mov_b32_e32 v65, v64
	s_nop 1
	v_permlane32_swap_b32_e32 v64, v65
	s_and_saveexec_b64 s[26:27], s[4:5]
	s_cbranch_execz .LBB0_1641
	v_or_b32_e32 v66, 48, v216
	v_ashrrev_i32_e32 v67, 31, v66
	v_add_f32_e32 v68, v64, v65
	v_lshlrev_b64 v[64:65], 7, v[66:67]
	v_lshl_add_u64 v[64:65], s[66:67], 0, v[64:65]
	v_lshl_add_u64 v[64:65], s[24:25], 2, v[64:65]
	s_lshl_b32 s94, s38, 2
	v_lshl_add_u64 v[64:65], v[64:65], 0, s[94:95]
	global_store_dword v[64:65], v68, off
.LBB0_1641:
	s_or_b64 exec, exec, s[26:27]
	s_mov_b64 s[0:1], 0x40000
	v_lshl_add_u64 v[76:77], v[218:219], 0, s[0:1]
	s_mov_b64 s[26:27], -1
	s_and_b64 vcc, exec, s[6:7]
	v_lshl_add_u64 v[72:73], v[76:77], 2, s[8:9]
	s_cbranch_vccnz .LBB0_1643
	global_load_dwordx4 v[68:71], v[72:73], off offset:16
	global_load_dwordx4 v[64:67], v[72:73], off
	s_waitcnt vmcnt(0)
	s_mov_b64 s[26:27], 0
.LBB0_1643:
	s_andn2_b64 vcc, exec, s[26:27]
	s_cbranch_vccnz .LBB0_1645
	s_waitcnt vmcnt(19)
	v_lshlrev_b32_e32 v64, 16, v148
	v_and_b32_e32 v65, 0xffff0000, v148
	v_lshlrev_b32_e32 v66, 16, v149
	v_and_b32_e32 v67, 0xffff0000, v149
	v_lshlrev_b32_e32 v68, 16, v150
	v_and_b32_e32 v69, 0xffff0000, v150
	v_lshlrev_b32_e32 v70, 16, v151
	v_and_b32_e32 v71, 0xffff0000, v151
.LBB0_1645:
	v_pk_add_f32 v[74:75], v[62:63], v[66:67]
	v_pk_add_f32 v[78:79], v[60:61], v[64:65]
	v_pk_add_f32 v[66:67], v[58:59], v[70:71]
	v_pk_add_f32 v[68:69], v[56:57], v[68:69]
	v_cvt_pk_bf16_f32 v56, v78, v79
	v_cvt_pk_bf16_f32 v57, v74, v75
	v_lshl_add_u64 v[64:65], v[76:77], 1, s[70:71]
	v_cvt_pk_bf16_f32 v58, v68, v69
	v_cvt_pk_bf16_f32 v59, v66, v67
	s_and_b64 vcc, exec, s[6:7]
	s_mov_b64 s[26:27], -1
	global_store_dwordx4 v[64:65], v[56:59], off
	s_cbranch_vccnz .LBB0_1647
	global_load_dwordx4 v[60:63], v[72:73], off offset:528
	global_load_dwordx4 v[56:59], v[72:73], off offset:512
	s_waitcnt vmcnt(0)
	s_mov_b64 s[26:27], 0
.LBB0_1647:
	s_andn2_b64 vcc, exec, s[26:27]
	s_cbranch_vccnz .LBB0_1649
	s_waitcnt vmcnt(19)
	v_lshlrev_b32_e32 v56, 16, v140
	v_and_b32_e32 v57, 0xffff0000, v140
	v_lshlrev_b32_e32 v58, 16, v141
	v_and_b32_e32 v59, 0xffff0000, v141
	v_lshlrev_b32_e32 v60, 16, v142
	v_and_b32_e32 v61, 0xffff0000, v142
	v_lshlrev_b32_e32 v62, 16, v143
	v_and_b32_e32 v63, 0xffff0000, v143
.LBB0_1649:
	v_pk_add_f32 v[54:55], v[54:55], v[58:59]
	v_pk_add_f32 v[52:53], v[52:53], v[56:57]
	v_pk_add_f32 v[58:59], v[48:49], v[60:61]
	v_cvt_pk_bf16_f32 v48, v52, v53
	v_cvt_pk_bf16_f32 v49, v54, v55
	v_pk_add_f32 v[56:57], v[50:51], v[62:63]
	v_cvt_pk_bf16_f32 v50, v58, v59
	v_mul_f32_e32 v70, v79, v79
	v_cvt_pk_bf16_f32 v51, v56, v57
	global_store_dwordx4 v[64:65], v[48:51], off offset:256
	v_mul_f32_e32 v71, v75, v75
	v_fmac_f32_e32 v70, v78, v78
	v_mul_f32_e32 v48, v53, v53
	v_mul_f32_e32 v49, v55, v55
	v_fmac_f32_e32 v48, v52, v52
	v_fmac_f32_e32 v49, v54, v54
	v_add_f32_e32 v48, v48, v49
	v_mul_f32_e32 v49, v59, v59
	v_fmac_f32_e32 v71, v74, v74
	v_mul_f32_e32 v69, v69, v69
	v_fmac_f32_e32 v49, v58, v58
	v_add_f32_e32 v70, v70, v71
	v_fmac_f32_e32 v69, v68, v68
	v_mul_f32_e32 v67, v67, v67
	v_add_f32_e32 v48, v49, v48
	v_mul_f32_e32 v49, v57, v57
	v_add_f32_e32 v68, v69, v70
	v_fmac_f32_e32 v67, v66, v66
	v_fmac_f32_e32 v49, v56, v56
	v_add_f32_e32 v66, v67, v68
	v_add_f32_e32 v48, v49, v48
	v_add_f32_e32 v48, v66, v48
	v_mov_b32_e32 v49, v48
	s_nop 1
	v_permlane16_swap_b32_e32 v48, v49
	v_add_f32_e32 v48, v48, v49
	v_mov_b32_e32 v49, v48
	s_nop 1
	v_permlane32_swap_b32_e32 v48, v49
	s_and_saveexec_b64 s[26:27], s[4:5]
	s_cbranch_execz .LBB0_1651
	v_add_u32_e32 v50, 0x80, v216
	v_ashrrev_i32_e32 v51, 31, v50
	v_add_f32_e32 v52, v48, v49
	v_lshlrev_b64 v[48:49], 7, v[50:51]
	v_lshl_add_u64 v[48:49], s[66:67], 0, v[48:49]
	v_lshl_add_u64 v[48:49], s[24:25], 2, v[48:49]
	s_lshl_b32 s94, s38, 2
	v_lshl_add_u64 v[48:49], v[48:49], 0, s[94:95]
	global_store_dword v[48:49], v52, off
.LBB0_1651:
	s_or_b64 exec, exec, s[26:27]
	s_mov_b64 s[0:1], 0x48000
	v_lshl_add_u64 v[60:61], v[218:219], 0, s[0:1]
	s_mov_b64 s[26:27], -1
	s_and_b64 vcc, exec, s[6:7]
	v_lshl_add_u64 v[56:57], v[60:61], 2, s[8:9]
	s_cbranch_vccnz .LBB0_1653
	global_load_dwordx4 v[52:55], v[56:57], off offset:16
	global_load_dwordx4 v[48:51], v[56:57], off
	s_waitcnt vmcnt(0)
	s_mov_b64 s[26:27], 0
.LBB0_1653:
	s_andn2_b64 vcc, exec, s[26:27]
	s_cbranch_vccnz .LBB0_1655
	s_waitcnt vmcnt(20)
	v_lshlrev_b32_e32 v48, 16, v128
	v_and_b32_e32 v49, 0xffff0000, v128
	v_lshlrev_b32_e32 v50, 16, v129
	v_and_b32_e32 v51, 0xffff0000, v129
	v_lshlrev_b32_e32 v52, 16, v130
	v_and_b32_e32 v53, 0xffff0000, v130
	v_lshlrev_b32_e32 v54, 16, v131
	v_and_b32_e32 v55, 0xffff0000, v131
.LBB0_1655:
	v_pk_add_f32 v[58:59], v[46:47], v[50:51]
	v_pk_add_f32 v[62:63], v[44:45], v[48:49]
	v_pk_add_f32 v[50:51], v[42:43], v[54:55]
	v_pk_add_f32 v[52:53], v[40:41], v[52:53]
	v_cvt_pk_bf16_f32 v40, v62, v63
	v_cvt_pk_bf16_f32 v41, v58, v59
	v_lshl_add_u64 v[48:49], v[60:61], 1, s[70:71]
	v_cvt_pk_bf16_f32 v42, v52, v53
	v_cvt_pk_bf16_f32 v43, v50, v51
	s_and_b64 vcc, exec, s[6:7]
	s_mov_b64 s[26:27], -1
	global_store_dwordx4 v[48:49], v[40:43], off
	s_cbranch_vccnz .LBB0_1657
	global_load_dwordx4 v[44:47], v[56:57], off offset:528
	global_load_dwordx4 v[40:43], v[56:57], off offset:512
	s_waitcnt vmcnt(0)
	s_mov_b64 s[26:27], 0
.LBB0_1657:
	s_andn2_b64 vcc, exec, s[26:27]
	s_cbranch_vccnz .LBB0_1659
	s_waitcnt vmcnt(20)
	v_lshlrev_b32_e32 v40, 16, v120
	v_and_b32_e32 v41, 0xffff0000, v120
	v_lshlrev_b32_e32 v42, 16, v121
	v_and_b32_e32 v43, 0xffff0000, v121
	v_lshlrev_b32_e32 v44, 16, v122
	v_and_b32_e32 v45, 0xffff0000, v122
	v_lshlrev_b32_e32 v46, 16, v123
	v_and_b32_e32 v47, 0xffff0000, v123
.LBB0_1659:
	v_pk_add_f32 v[38:39], v[38:39], v[42:43]
	v_pk_add_f32 v[36:37], v[36:37], v[40:41]
	v_pk_add_f32 v[42:43], v[32:33], v[44:45]
	v_cvt_pk_bf16_f32 v32, v36, v37
	v_cvt_pk_bf16_f32 v33, v38, v39
	v_pk_add_f32 v[40:41], v[34:35], v[46:47]
	v_cvt_pk_bf16_f32 v34, v42, v43
	v_mul_f32_e32 v54, v63, v63
	v_cvt_pk_bf16_f32 v35, v40, v41
	global_store_dwordx4 v[48:49], v[32:35], off offset:256
	v_mul_f32_e32 v55, v59, v59
	v_fmac_f32_e32 v54, v62, v62
	v_mul_f32_e32 v32, v37, v37
	v_mul_f32_e32 v33, v39, v39
	v_fmac_f32_e32 v32, v36, v36
	v_fmac_f32_e32 v33, v38, v38
	v_add_f32_e32 v32, v32, v33
	v_mul_f32_e32 v33, v43, v43
	v_fmac_f32_e32 v55, v58, v58
	v_mul_f32_e32 v53, v53, v53
	v_fmac_f32_e32 v33, v42, v42
	v_add_f32_e32 v54, v54, v55
	v_fmac_f32_e32 v53, v52, v52
	v_mul_f32_e32 v51, v51, v51
	v_add_f32_e32 v32, v33, v32
	v_mul_f32_e32 v33, v41, v41
	v_add_f32_e32 v52, v53, v54
	v_fmac_f32_e32 v51, v50, v50
	v_fmac_f32_e32 v33, v40, v40
	v_add_f32_e32 v50, v51, v52
	v_add_f32_e32 v32, v33, v32
	v_add_f32_e32 v32, v50, v32
	v_mov_b32_e32 v33, v32
	s_nop 1
	v_permlane16_swap_b32_e32 v32, v33
	v_add_f32_e32 v32, v32, v33
	v_mov_b32_e32 v33, v32
	s_nop 1
	v_permlane32_swap_b32_e32 v32, v33
	s_and_saveexec_b64 s[26:27], s[4:5]
	s_cbranch_execz .LBB0_1661
	v_add_u32_e32 v34, 0x90, v216
	v_ashrrev_i32_e32 v35, 31, v34
	v_add_f32_e32 v36, v32, v33
	v_lshlrev_b64 v[32:33], 7, v[34:35]
	v_lshl_add_u64 v[32:33], s[66:67], 0, v[32:33]
	v_lshl_add_u64 v[32:33], s[24:25], 2, v[32:33]
	s_lshl_b32 s94, s38, 2
	v_lshl_add_u64 v[32:33], v[32:33], 0, s[94:95]
	global_store_dword v[32:33], v36, off
.LBB0_1661:
	s_or_b64 exec, exec, s[26:27]
	s_mov_b64 s[0:1], 0x50000
	v_lshl_add_u64 v[44:45], v[218:219], 0, s[0:1]
	s_mov_b64 s[26:27], -1
	s_and_b64 vcc, exec, s[6:7]
	v_lshl_add_u64 v[40:41], v[44:45], 2, s[8:9]
	s_cbranch_vccnz .LBB0_1663
	global_load_dwordx4 v[36:39], v[40:41], off offset:16
	global_load_dwordx4 v[32:35], v[40:41], off
	s_waitcnt vmcnt(0)
	s_mov_b64 s[26:27], 0
.LBB0_1663:
	s_andn2_b64 vcc, exec, s[26:27]
	s_cbranch_vccnz .LBB0_1665
	s_waitcnt vmcnt(21)
	v_lshlrev_b32_e32 v32, 16, v108
	v_and_b32_e32 v33, 0xffff0000, v108
	v_lshlrev_b32_e32 v34, 16, v109
	v_and_b32_e32 v35, 0xffff0000, v109
	v_lshlrev_b32_e32 v36, 16, v110
	v_and_b32_e32 v37, 0xffff0000, v110
	v_lshlrev_b32_e32 v38, 16, v111
	v_and_b32_e32 v39, 0xffff0000, v111
.LBB0_1665:
	v_pk_add_f32 v[42:43], v[30:31], v[34:35]
	v_pk_add_f32 v[46:47], v[28:29], v[32:33]
	v_pk_add_f32 v[34:35], v[26:27], v[38:39]
	v_pk_add_f32 v[36:37], v[24:25], v[36:37]
	v_cvt_pk_bf16_f32 v24, v46, v47
	v_cvt_pk_bf16_f32 v25, v42, v43
	v_lshl_add_u64 v[32:33], v[44:45], 1, s[70:71]
	v_cvt_pk_bf16_f32 v26, v36, v37
	v_cvt_pk_bf16_f32 v27, v34, v35
	s_and_b64 vcc, exec, s[6:7]
	s_mov_b64 s[26:27], -1
	global_store_dwordx4 v[32:33], v[24:27], off
	s_cbranch_vccnz .LBB0_1667
	global_load_dwordx4 v[28:31], v[40:41], off offset:528
	global_load_dwordx4 v[24:27], v[40:41], off offset:512
	s_waitcnt vmcnt(0)
	s_mov_b64 s[26:27], 0
.LBB0_1667:
	s_andn2_b64 vcc, exec, s[26:27]
	s_cbranch_vccnz .LBB0_1669
	s_waitcnt vmcnt(21)
	v_lshlrev_b32_e32 v24, 16, v96
	v_and_b32_e32 v25, 0xffff0000, v96
	v_lshlrev_b32_e32 v26, 16, v97
	v_and_b32_e32 v27, 0xffff0000, v97
	v_lshlrev_b32_e32 v28, 16, v98
	v_and_b32_e32 v29, 0xffff0000, v98
	v_lshlrev_b32_e32 v30, 16, v99
	v_and_b32_e32 v31, 0xffff0000, v99
.LBB0_1669:
	v_pk_add_f32 v[22:23], v[22:23], v[26:27]
	v_pk_add_f32 v[20:21], v[20:21], v[24:25]
	v_pk_add_f32 v[26:27], v[16:17], v[28:29]
	v_cvt_pk_bf16_f32 v16, v20, v21
	v_cvt_pk_bf16_f32 v17, v22, v23
	v_pk_add_f32 v[24:25], v[18:19], v[30:31]
	v_cvt_pk_bf16_f32 v18, v26, v27
	v_mul_f32_e32 v38, v47, v47
	v_cvt_pk_bf16_f32 v19, v24, v25
	global_store_dwordx4 v[32:33], v[16:19], off offset:256
	v_mul_f32_e32 v39, v43, v43
	v_fmac_f32_e32 v38, v46, v46
	v_mul_f32_e32 v16, v21, v21
	v_mul_f32_e32 v17, v23, v23
	v_fmac_f32_e32 v16, v20, v20
	v_fmac_f32_e32 v17, v22, v22
	v_add_f32_e32 v16, v16, v17
	v_mul_f32_e32 v17, v27, v27
	v_fmac_f32_e32 v39, v42, v42
	v_mul_f32_e32 v37, v37, v37
	v_fmac_f32_e32 v17, v26, v26
	v_add_f32_e32 v38, v38, v39
	v_fmac_f32_e32 v37, v36, v36
	v_mul_f32_e32 v35, v35, v35
	v_add_f32_e32 v16, v17, v16
	v_mul_f32_e32 v17, v25, v25
	v_add_f32_e32 v36, v37, v38
	v_fmac_f32_e32 v35, v34, v34
	v_fmac_f32_e32 v17, v24, v24
	v_add_f32_e32 v34, v35, v36
	v_add_f32_e32 v16, v17, v16
	v_add_f32_e32 v16, v34, v16
	v_mov_b32_e32 v17, v16
	s_nop 1
	v_permlane16_swap_b32_e32 v16, v17
	v_add_f32_e32 v16, v16, v17
	v_mov_b32_e32 v17, v16
	s_nop 1
	v_permlane32_swap_b32_e32 v16, v17
	s_and_saveexec_b64 s[26:27], s[4:5]
	s_cbranch_execz .LBB0_1671
	v_add_u32_e32 v18, 0xa0, v216
	v_ashrrev_i32_e32 v19, 31, v18
	v_add_f32_e32 v20, v16, v17
	v_lshlrev_b64 v[16:17], 7, v[18:19]
	v_lshl_add_u64 v[16:17], s[66:67], 0, v[16:17]
	v_lshl_add_u64 v[16:17], s[24:25], 2, v[16:17]
	s_lshl_b32 s94, s38, 2
	v_lshl_add_u64 v[16:17], v[16:17], 0, s[94:95]
	global_store_dword v[16:17], v20, off
.LBB0_1671:
	s_or_b64 exec, exec, s[26:27]
	s_mov_b64 s[0:1], 0x58000
	v_lshl_add_u64 v[28:29], v[218:219], 0, s[0:1]
	s_mov_b64 s[26:27], -1
	s_and_b64 vcc, exec, s[6:7]
	v_lshl_add_u64 v[24:25], v[28:29], 2, s[8:9]
	s_cbranch_vccnz .LBB0_1673
	global_load_dwordx4 v[20:23], v[24:25], off offset:16
	global_load_dwordx4 v[16:19], v[24:25], off
	s_waitcnt vmcnt(0)
	s_mov_b64 s[26:27], 0
.LBB0_1673:
	s_andn2_b64 vcc, exec, s[26:27]
	s_cbranch_vccnz .LBB0_1675
	s_waitcnt vmcnt(22)
	v_lshlrev_b32_e32 v16, 16, v88
	v_and_b32_e32 v17, 0xffff0000, v88
	v_lshlrev_b32_e32 v18, 16, v89
	v_and_b32_e32 v19, 0xffff0000, v89
	v_lshlrev_b32_e32 v20, 16, v90
	v_and_b32_e32 v21, 0xffff0000, v90
	v_lshlrev_b32_e32 v22, 16, v91
	v_and_b32_e32 v23, 0xffff0000, v91
.LBB0_1675:
	v_pk_add_f32 v[26:27], v[14:15], v[18:19]
	v_pk_add_f32 v[30:31], v[12:13], v[16:17]
	v_pk_add_f32 v[18:19], v[10:11], v[22:23]
	v_pk_add_f32 v[20:21], v[8:9], v[20:21]
	v_cvt_pk_bf16_f32 v8, v30, v31
	v_cvt_pk_bf16_f32 v9, v26, v27
	v_lshl_add_u64 v[16:17], v[28:29], 1, s[70:71]
	v_cvt_pk_bf16_f32 v10, v20, v21
	v_cvt_pk_bf16_f32 v11, v18, v19
	s_and_b64 vcc, exec, s[6:7]
	s_mov_b64 s[6:7], -1
	global_store_dwordx4 v[16:17], v[8:11], off
	s_cbranch_vccnz .LBB0_1677
	global_load_dwordx4 v[12:15], v[24:25], off offset:528
	global_load_dwordx4 v[8:11], v[24:25], off offset:512
	s_waitcnt vmcnt(0)
	s_mov_b64 s[6:7], 0
.LBB0_1677:
	s_andn2_b64 vcc, exec, s[6:7]
	s_cbranch_vccnz .LBB0_1679
	s_waitcnt vmcnt(22)
	v_lshlrev_b32_e32 v8, 16, v80
	v_and_b32_e32 v9, 0xffff0000, v80
	v_lshlrev_b32_e32 v10, 16, v81
	v_and_b32_e32 v11, 0xffff0000, v81
	v_lshlrev_b32_e32 v12, 16, v82
	v_and_b32_e32 v13, 0xffff0000, v82
	v_lshlrev_b32_e32 v14, 16, v83
	v_and_b32_e32 v15, 0xffff0000, v83
.LBB0_1679:
	v_pk_add_f32 v[6:7], v[6:7], v[10:11]
	v_pk_add_f32 v[4:5], v[4:5], v[8:9]
	v_pk_add_f32 v[10:11], v[0:1], v[12:13]
	v_cvt_pk_bf16_f32 v0, v4, v5
	v_cvt_pk_bf16_f32 v1, v6, v7
	v_pk_add_f32 v[8:9], v[2:3], v[14:15]
	v_cvt_pk_bf16_f32 v2, v10, v11
	v_mul_f32_e32 v22, v31, v31
	v_cvt_pk_bf16_f32 v3, v8, v9
	global_store_dwordx4 v[16:17], v[0:3], off offset:256
	v_mul_f32_e32 v23, v27, v27
	v_fmac_f32_e32 v22, v30, v30
	v_mul_f32_e32 v0, v5, v5
	v_mul_f32_e32 v1, v7, v7
	v_fmac_f32_e32 v0, v4, v4
	v_fmac_f32_e32 v1, v6, v6
	v_add_f32_e32 v0, v0, v1
	v_mul_f32_e32 v1, v11, v11
	v_fmac_f32_e32 v23, v26, v26
	v_mul_f32_e32 v21, v21, v21
	v_fmac_f32_e32 v1, v10, v10
	v_add_f32_e32 v22, v22, v23
	v_fmac_f32_e32 v21, v20, v20
	v_mul_f32_e32 v19, v19, v19
	v_add_f32_e32 v0, v1, v0
	v_mul_f32_e32 v1, v9, v9
	v_add_f32_e32 v20, v21, v22
	v_fmac_f32_e32 v19, v18, v18
	v_fmac_f32_e32 v1, v8, v8
	v_add_f32_e32 v18, v19, v20
	v_add_f32_e32 v0, v1, v0
	v_add_f32_e32 v0, v18, v0
	v_mov_b32_e32 v1, v0
	s_nop 1
	v_permlane16_swap_b32_e32 v0, v1
	v_add_f32_e32 v0, v0, v1
	v_mov_b32_e32 v1, v0
	s_nop 1
	v_permlane32_swap_b32_e32 v0, v1
	s_and_saveexec_b64 s[6:7], s[4:5]
	s_cbranch_execz .LBB0_1681
	v_add_u32_e32 v2, 0xb0, v216
	v_ashrrev_i32_e32 v3, 31, v2
	v_add_f32_e32 v4, v0, v1
	v_lshlrev_b64 v[0:1], 7, v[2:3]
	v_lshl_add_u64 v[0:1], s[66:67], 0, v[0:1]
	v_lshl_add_u64 v[0:1], s[24:25], 2, v[0:1]
	s_lshl_b32 s94, s38, 2
	v_lshl_add_u64 v[0:1], v[0:1], 0, s[94:95]
	global_store_dword v[0:1], v4, off
